# v30 + P8 epilogue relu/square/clamp as med3(t,0,sqrt448)+square (identical fp8 outputs)
# speedup vs baseline: 1.0137x; 1.0044x over previous
; __device__ __forceinline__ unsigned pk4_fp8(float a, float b, float c, float d) {
;     a = fminf(fmaxf(a, -448.f), 448.f); b = fminf(fmaxf(b, -448.f), 448.f); c = fminf(fmaxf(c, -448.f), 448.f); d = fminf(fmaxf(d, -448.f), 448.f);
;     int w = 0; w = __builtin_amdgcn_cvt_pk_fp8_f32(a, b, w, false); w = __builtin_amdgcn_cvt_pk_fp8_f32(c, d, w, true); return (unsigned)w;
;     __device__ __forceinline__ void operator()(const f32x4 (&acc)[2][2][4][2], const Unit& u, int wr, int wc, int fr, int fq) const {
;         const int row0 = u.pm * BM + wr * 64 + fr, col0 = u.pn * BM + wc * 32 + 8 * fq;
; #pragma unroll
;         for (int ai = 0; ai < 2; ++ai)
; #pragma unroll
;             for (int m = 0; m < 4; ++m) {
;                 const int row = row0 + ai * HALF + m * 16;
;                 const float rs = rsqrtf(ss[row] * (1.0f / 4096.0f) + RMS_EPS) * (1.0f / 64.0f);
;                 unsigned char* rowp = U + ((size_t)(row >> 4) * 512 + (col0 >> 5)) * 512 + (row & 15) * 32 + (col0 & 31);
; #pragma unroll
;                 for (int bj = 0; bj < 2; ++bj) {
;                     f32x4 v0 = acc[ai][bj][m][0] * rs, v1 = acc[ai][bj][m][1] * rs;
; #pragma unroll
;                     for (int j = 0; j < 4; ++j) { const float a = fmaxf(v0[j], 0.f), b = fmaxf(v1[j], 0.f); v0[j] = a * a * 4.f; v1[j] = b * b * 4.f; }
;                     u32x2 w; w.x = pk4_fp8(v0[0], v0[1], v0[2], v0[3]); w.y = pk4_fp8(v1[0], v1[1], v1[2], v1[3]);
;                     *(u32x2*)(rowp + bj * (HALF / 32) * 512) = w;
;                 }
.LBB0_2284:
	s_mov_b32 s99, 0x41a953fd
	s_lshl_b32 s13, s20, 8
	s_add_i32 s13, s13, s36
	v_or_b32_e32 v2, s13, v1
	v_ashrrev_i32_e32 v3, 31, v2
	s_nop 15
	s_nop 15
	v_lshl_add_u64 v[4:5], v[2:3], 2, s[2:3]
	s_lshl_b32 s15, s21, 8
	s_or_b32 s15, s15, s37
	s_ashr_i32 s20, s15, 5
	s_ashr_i32 s22, s13, 4
	s_ashr_i32 s21, s20, 31
	s_ashr_i32 s23, s22, 31
	s_lshl_b64 s[20:21], s[20:21], 9
	s_lshl_b64 s[22:23], s[22:23], 18
	v_readlane_b32 s24, v253, 46
	v_readlane_b32 s25, v253, 47
	s_add_u32 s13, s24, s22
	s_addc_u32 s15, s25, s23
	s_add_u32 s22, s13, s20
	s_addc_u32 s23, s15, s21
	s_waitcnt vmcnt(0)
	v_fmamk_f32 v3, v234, 0x39800000, v194
	v_mul_f32_e32 v9, 0x4b800000, v3
	v_cmp_gt_f32_e32 vcc, s43, v3
	s_nop 1
	v_cndmask_b32_e32 v3, v3, v9, vcc
	v_rsq_f32_e32 v3, v3
	s_nop 0
	v_mul_f32_e32 v9, 0x45800000, v3
	v_cndmask_b32_e32 v3, v3, v9, vcc
	v_mul_f32_e32 v10, 0x3d000000, v3
	v_pk_mul_f32 v[14:15], v[158:159], v[10:11] op_sel_hi:[1,0]
	v_pk_mul_f32 v[18:19], v[154:155], v[10:11] op_sel_hi:[1,0]
	v_pk_mul_f32 v[12:13], v[160:161], v[10:11] op_sel_hi:[1,0]
	v_pk_mul_f32 v[16:17], v[156:157], v[10:11] op_sel_hi:[1,0]
	v_pk_mul_f32 v[20:21], v[152:153], v[10:11] op_sel_hi:[1,0]
	v_pk_mul_f32 v[22:23], v[150:151], v[10:11] op_sel_hi:[1,0]
	v_pk_mul_f32 v[24:25], v[148:149], v[10:11] op_sel_hi:[1,0]
	v_pk_mul_f32 v[10:11], v[146:147], v[10:11] op_sel_hi:[1,0]
	v_med3_f32 v3, v14, 0, s99
	v_med3_f32 v9, v18, 0, s99
	v_med3_f32 v14, v15, 0, s99
	v_med3_f32 v15, v19, 0, s99
	v_med3_f32 v18, v22, 0, s99
	v_med3_f32 v10, v10, 0, s99
	v_med3_f32 v19, v23, 0, s99
	v_med3_f32 v11, v11, 0, s99
	v_mul_f32_e32 v3, v3, v3
	v_mul_f32_e32 v9, v9, v9
	v_mul_f32_e32 v14, v14, v14
	v_mul_f32_e32 v15, v15, v15
	v_mul_f32_e32 v18, v18, v18
	v_mul_f32_e32 v10, v10, v10
	v_mul_f32_e32 v19, v19, v19
	v_mul_f32_e32 v11, v11, v11
	v_med3_f32 v12, v12, 0, s99
	v_med3_f32 v16, v16, 0, s99
	v_med3_f32 v13, v13, 0, s99
	v_med3_f32 v17, v17, 0, s99
	v_cvt_pk_fp8_f32 v6, v3, v14
	v_cvt_pk_fp8_f32 v7, v9, v15
	v_mov_b32_e32 v3, v11
	v_med3_f32 v20, v20, 0, s99
	v_med3_f32 v22, v24, 0, s99
	v_med3_f32 v21, v21, 0, s99
	v_med3_f32 v23, v25, 0, s99
	v_mul_f32_e32 v12, v12, v12
	v_mul_f32_e32 v16, v16, v16
	v_mul_f32_e32 v13, v13, v13
	v_mul_f32_e32 v17, v17, v17
	v_cvt_pk_fp8_f32 v8, v18, v19
	v_cvt_pk_fp8_f32 v9, v10, v3
	v_mul_f32_e32 v20, v20, v20
	v_mul_f32_e32 v22, v22, v22
	v_mul_f32_e32 v21, v21, v21
	v_mul_f32_e32 v23, v23, v23
	v_cvt_pk_fp8_f32 v6, v12, v13 op_sel:[0,0,1]
	v_cvt_pk_fp8_f32 v7, v16, v17 op_sel:[0,0,1]
	v_mov_b32_e32 v3, v22
	v_mov_b32_e32 v10, v23
	v_cvt_pk_fp8_f32 v8, v20, v21 op_sel:[0,0,1]
	v_cvt_pk_fp8_f32 v9, v3, v10 op_sel:[0,0,1]
	v_lshl_add_u64 v[10:11], s[22:23], 0, v[172:173]
	v_lshl_add_u64 v[10:11], v[10:11], 0, v[170:171]
	global_store_dwordx2 v[10:11], v[6:7], off
	global_store_dwordx2 v[10:11], v[8:9], off offset:2048
	v_or_b32_e32 v6, 16, v2
	v_ashrrev_i32_e32 v7, 31, v6
	v_lshl_add_u64 v[8:9], v[6:7], 2, s[2:3]
	v_ashrrev_i32_e32 v6, 4, v6
	v_ashrrev_i32_e32 v7, 31, v6
	v_lshlrev_b64 v[6:7], 18, v[6:7]
	v_lshl_add_u64 v[6:7], s[24:25], 0, v[6:7]
	v_lshl_add_u64 v[6:7], v[6:7], 0, s[20:21]
	v_lshl_add_u64 v[6:7], v[6:7], 0, v[172:173]
	v_lshl_add_u64 v[6:7], v[6:7], 0, v[170:171]
	v_fmamk_f32 v3, v235, 0x39800000, v194
	v_mul_f32_e32 v11, 0x4b800000, v3
	v_cmp_gt_f32_e32 vcc, s43, v3
	s_nop 1
	v_cndmask_b32_e32 v3, v3, v11, vcc
	v_rsq_f32_e32 v3, v3
	s_nop 0
	v_mul_f32_e32 v11, 0x45800000, v3
	v_cndmask_b32_e32 v3, v3, v11, vcc
	v_mul_f32_e32 v12, 0x3d000000, v3
	v_pk_mul_f32 v[16:17], v[142:143], v[12:13] op_sel_hi:[1,0]
	v_pk_mul_f32 v[20:21], v[138:139], v[12:13] op_sel_hi:[1,0]
	v_pk_mul_f32 v[14:15], v[144:145], v[12:13] op_sel_hi:[1,0]
	v_pk_mul_f32 v[18:19], v[140:141], v[12:13] op_sel_hi:[1,0]
	v_pk_mul_f32 v[22:23], v[136:137], v[12:13] op_sel_hi:[1,0]
	v_pk_mul_f32 v[24:25], v[134:135], v[12:13] op_sel_hi:[1,0]
	v_pk_mul_f32 v[26:27], v[132:133], v[12:13] op_sel_hi:[1,0]
	v_pk_mul_f32 v[12:13], v[130:131], v[12:13] op_sel_hi:[1,0]
	v_med3_f32 v3, v16, 0, s99
	v_med3_f32 v11, v20, 0, s99
	v_med3_f32 v16, v17, 0, s99
	v_med3_f32 v17, v21, 0, s99
	v_med3_f32 v20, v24, 0, s99
	v_med3_f32 v12, v12, 0, s99
	v_med3_f32 v21, v25, 0, s99
	v_med3_f32 v13, v13, 0, s99
	v_mul_f32_e32 v3, v3, v3
	v_mul_f32_e32 v11, v11, v11
	v_mul_f32_e32 v16, v16, v16
	v_mul_f32_e32 v17, v17, v17
	v_mul_f32_e32 v20, v20, v20
	v_mul_f32_e32 v12, v12, v12
	v_mul_f32_e32 v21, v21, v21
	v_mul_f32_e32 v13, v13, v13
	v_med3_f32 v14, v14, 0, s99
	v_med3_f32 v18, v18, 0, s99
	v_med3_f32 v15, v15, 0, s99
	v_med3_f32 v19, v19, 0, s99
	v_cvt_pk_fp8_f32 v8, v3, v16
	v_cvt_pk_fp8_f32 v9, v11, v17
	v_mov_b32_e32 v3, v12
	v_mov_b32_e32 v12, v13
	v_med3_f32 v22, v22, 0, s99
	v_med3_f32 v24, v26, 0, s99
	v_med3_f32 v23, v23, 0, s99
	v_med3_f32 v25, v27, 0, s99
	v_mul_f32_e32 v14, v14, v14
	v_mul_f32_e32 v18, v18, v18
	v_mul_f32_e32 v15, v15, v15
	v_mul_f32_e32 v19, v19, v19
	v_cvt_pk_fp8_f32 v10, v20, v21
	v_cvt_pk_fp8_f32 v11, v3, v12
	v_mul_f32_e32 v22, v22, v22
	v_mul_f32_e32 v24, v24, v24
	v_mul_f32_e32 v23, v23, v23
	v_mul_f32_e32 v25, v25, v25
	v_cvt_pk_fp8_f32 v8, v14, v15 op_sel:[0,0,1]
	v_cvt_pk_fp8_f32 v9, v18, v19 op_sel:[0,0,1]
	v_mov_b32_e32 v3, v24
	v_mov_b32_e32 v12, v25
	v_cvt_pk_fp8_f32 v10, v22, v23 op_sel:[0,0,1]
	v_cvt_pk_fp8_f32 v11, v3, v12 op_sel:[0,0,1]
	global_store_dwordx2 v[6:7], v[8:9], off
	global_store_dwordx2 v[6:7], v[10:11], off offset:2048
	v_or_b32_e32 v6, 32, v2
	v_ashrrev_i32_e32 v7, 31, v6
	v_lshl_add_u64 v[8:9], v[6:7], 2, s[2:3]
	v_ashrrev_i32_e32 v6, 4, v6
	v_ashrrev_i32_e32 v7, 31, v6
	v_lshlrev_b64 v[6:7], 18, v[6:7]
; __device__ __forceinline__ unsigned pk4_fp8(float a, float b, float c, float d) {
;     a = fminf(fmaxf(a, -448.f), 448.f); b = fminf(fmaxf(b, -448.f), 448.f); c = fminf(fmaxf(c, -448.f), 448.f); d = fminf(fmaxf(d, -448.f), 448.f);
;     int w = 0; w = __builtin_amdgcn_cvt_pk_fp8_f32(a, b, w, false); w = __builtin_amdgcn_cvt_pk_fp8_f32(c, d, w, true); return (unsigned)w;
;     __device__ __forceinline__ void operator()(const f32x4 (&acc)[2][2][4][2], const Unit& u, int wr, int wc, int fr, int fq) const {
;         const int row0 = u.pm * BM + wr * 64 + fr, col0 = u.pn * BM + wc * 32 + 8 * fq;
; #pragma unroll
;         for (int ai = 0; ai < 2; ++ai)
; #pragma unroll
;             for (int m = 0; m < 4; ++m) {
;                 const int row = row0 + ai * HALF + m * 16;
;                 const float rs = rsqrtf(ss[row] * (1.0f / 4096.0f) + RMS_EPS) * (1.0f / 64.0f);
;                 unsigned char* rowp = U + ((size_t)(row >> 4) * 512 + (col0 >> 5)) * 512 + (row & 15) * 32 + (col0 & 31);
; #pragma unroll
;                 for (int bj = 0; bj < 2; ++bj) {
;                     f32x4 v0 = acc[ai][bj][m][0] * rs, v1 = acc[ai][bj][m][1] * rs;
; #pragma unroll
;                     for (int j = 0; j < 4; ++j) { const float a = fmaxf(v0[j], 0.f), b = fmaxf(v1[j], 0.f); v0[j] = a * a * 4.f; v1[j] = b * b * 4.f; }
;                     u32x2 w; w.x = pk4_fp8(v0[0], v0[1], v0[2], v0[3]); w.y = pk4_fp8(v1[0], v1[1], v1[2], v1[3]);
;                     *(u32x2*)(rowp + bj * (HALF / 32) * 512) = w;
;                 }
	v_lshl_add_u64 v[6:7], s[24:25], 0, v[6:7]
	v_lshl_add_u64 v[6:7], v[6:7], 0, s[20:21]
	v_lshl_add_u64 v[6:7], v[6:7], 0, v[172:173]
	v_lshl_add_u64 v[6:7], v[6:7], 0, v[170:171]
	v_fmamk_f32 v3, v236, 0x39800000, v194
	v_mul_f32_e32 v11, 0x4b800000, v3
	v_cmp_gt_f32_e32 vcc, s43, v3
	s_nop 1
	v_cndmask_b32_e32 v3, v3, v11, vcc
	v_rsq_f32_e32 v3, v3
	s_nop 0
	v_mul_f32_e32 v11, 0x45800000, v3
	v_cndmask_b32_e32 v3, v3, v11, vcc
	v_mul_f32_e32 v12, 0x3d000000, v3
	v_pk_mul_f32 v[16:17], v[126:127], v[12:13] op_sel_hi:[1,0]
	v_pk_mul_f32 v[20:21], v[122:123], v[12:13] op_sel_hi:[1,0]
	v_pk_mul_f32 v[24:25], v[118:119], v[12:13] op_sel_hi:[1,0]
	v_pk_mul_f32 v[14:15], v[128:129], v[12:13] op_sel_hi:[1,0]
	v_pk_mul_f32 v[18:19], v[124:125], v[12:13] op_sel_hi:[1,0]
	v_pk_mul_f32 v[22:23], v[120:121], v[12:13] op_sel_hi:[1,0]
	v_pk_mul_f32 v[26:27], v[116:117], v[12:13] op_sel_hi:[1,0]
	v_pk_mul_f32 v[12:13], v[114:115], v[12:13] op_sel_hi:[1,0]
	v_med3_f32 v3, v16, 0, s99
	v_med3_f32 v11, v20, 0, s99
	v_med3_f32 v16, v17, 0, s99
	v_med3_f32 v17, v21, 0, s99
	v_med3_f32 v20, v24, 0, s99
	v_med3_f32 v21, v25, 0, s99
	v_med3_f32 v12, v12, 0, s99
	v_med3_f32 v13, v13, 0, s99
	v_mul_f32_e32 v3, v3, v3
	v_mul_f32_e32 v11, v11, v11
	v_mul_f32_e32 v16, v16, v16
	v_mul_f32_e32 v17, v17, v17
	v_mul_f32_e32 v20, v20, v20
	v_mul_f32_e32 v21, v21, v21
	v_mul_f32_e32 v12, v12, v12
	v_mul_f32_e32 v13, v13, v13
	v_med3_f32 v14, v14, 0, s99
	v_med3_f32 v18, v18, 0, s99
	v_med3_f32 v15, v15, 0, s99
	v_med3_f32 v19, v19, 0, s99
	v_med3_f32 v22, v22, 0, s99
	v_med3_f32 v23, v23, 0, s99
	v_cvt_pk_fp8_f32 v8, v3, v16
	v_cvt_pk_fp8_f32 v9, v11, v17
	v_cvt_pk_fp8_f32 v10, v20, v21
	v_med3_f32 v24, v26, 0, s99
	v_med3_f32 v25, v27, 0, s99
	v_mul_f32_e32 v14, v14, v14
	v_mul_f32_e32 v18, v18, v18
	v_mul_f32_e32 v15, v15, v15
	v_mul_f32_e32 v19, v19, v19
	v_mul_f32_e32 v22, v22, v22
	v_mul_f32_e32 v23, v23, v23
	v_cvt_pk_fp8_f32 v11, v12, v13
	v_mul_f32_e32 v24, v24, v24
	v_mul_f32_e32 v25, v25, v25
	v_mov_b32_e32 v3, v23
	v_cvt_pk_fp8_f32 v8, v14, v15 op_sel:[0,0,1]
	v_cvt_pk_fp8_f32 v9, v18, v19 op_sel:[0,0,1]
	v_cvt_pk_fp8_f32 v10, v22, v3 op_sel:[0,0,1]
	v_mov_b32_e32 v3, v24
	v_mov_b32_e32 v12, v25
	v_cvt_pk_fp8_f32 v11, v3, v12 op_sel:[0,0,1]
	global_store_dwordx2 v[6:7], v[8:9], off
	global_store_dwordx2 v[6:7], v[10:11], off offset:2048
	v_or_b32_e32 v6, 48, v2
	v_ashrrev_i32_e32 v7, 31, v6
	v_lshl_add_u64 v[8:9], v[6:7], 2, s[2:3]
	v_ashrrev_i32_e32 v6, 4, v6
	v_ashrrev_i32_e32 v7, 31, v6
	v_lshlrev_b64 v[6:7], 18, v[6:7]
	v_lshl_add_u64 v[6:7], s[24:25], 0, v[6:7]
	v_lshl_add_u64 v[6:7], v[6:7], 0, s[20:21]
	v_lshl_add_u64 v[6:7], v[6:7], 0, v[172:173]
	v_lshl_add_u64 v[6:7], v[6:7], 0, v[170:171]
	v_fmamk_f32 v3, v237, 0x39800000, v194
	v_mul_f32_e32 v11, 0x4b800000, v3
	v_cmp_gt_f32_e32 vcc, s43, v3
	s_nop 1
	v_cndmask_b32_e32 v3, v3, v11, vcc
	v_rsq_f32_e32 v3, v3
	s_nop 0
	v_mul_f32_e32 v11, 0x45800000, v3
	v_cndmask_b32_e32 v3, v3, v11, vcc
	v_mul_f32_e32 v12, 0x3d000000, v3
	v_pk_mul_f32 v[16:17], v[110:111], v[12:13] op_sel_hi:[1,0]
	v_pk_mul_f32 v[20:21], v[106:107], v[12:13] op_sel_hi:[1,0]
	v_pk_mul_f32 v[24:25], v[102:103], v[12:13] op_sel_hi:[1,0]
	v_pk_mul_f32 v[14:15], v[112:113], v[12:13] op_sel_hi:[1,0]
	v_pk_mul_f32 v[18:19], v[108:109], v[12:13] op_sel_hi:[1,0]
	v_pk_mul_f32 v[22:23], v[104:105], v[12:13] op_sel_hi:[1,0]
	v_pk_mul_f32 v[26:27], v[100:101], v[12:13] op_sel_hi:[1,0]
	v_pk_mul_f32 v[12:13], v[98:99], v[12:13] op_sel_hi:[1,0]
	v_med3_f32 v3, v16, 0, s99
	v_med3_f32 v11, v20, 0, s99
	v_med3_f32 v16, v17, 0, s99
	v_med3_f32 v17, v21, 0, s99
	v_med3_f32 v20, v24, 0, s99
	v_med3_f32 v21, v25, 0, s99
	v_med3_f32 v12, v12, 0, s99
	v_med3_f32 v13, v13, 0, s99
	v_mul_f32_e32 v3, v3, v3
	v_mul_f32_e32 v11, v11, v11
	v_mul_f32_e32 v16, v16, v16
	v_mul_f32_e32 v17, v17, v17
	v_mul_f32_e32 v20, v20, v20
	v_mul_f32_e32 v21, v21, v21
	v_mul_f32_e32 v12, v12, v12
	v_mul_f32_e32 v13, v13, v13
	v_med3_f32 v14, v14, 0, s99
	v_med3_f32 v18, v18, 0, s99
	v_med3_f32 v15, v15, 0, s99
	v_med3_f32 v19, v19, 0, s99
	v_med3_f32 v22, v22, 0, s99
	v_med3_f32 v23, v23, 0, s99
	v_cvt_pk_fp8_f32 v8, v3, v16
	v_cvt_pk_fp8_f32 v9, v11, v17
	v_cvt_pk_fp8_f32 v10, v20, v21
	v_med3_f32 v24, v26, 0, s99
	v_med3_f32 v25, v27, 0, s99
	v_mul_f32_e32 v14, v14, v14
	v_mul_f32_e32 v18, v18, v18
	v_mul_f32_e32 v15, v15, v15
	v_mul_f32_e32 v19, v19, v19
	v_mul_f32_e32 v22, v22, v22
	v_mul_f32_e32 v23, v23, v23
	v_cvt_pk_fp8_f32 v11, v12, v13
	v_mul_f32_e32 v24, v24, v24
	v_mul_f32_e32 v25, v25, v25
	v_mov_b32_e32 v3, v22
	v_mov_b32_e32 v16, v23
	v_cvt_pk_fp8_f32 v8, v14, v15 op_sel:[0,0,1]
	v_cvt_pk_fp8_f32 v9, v18, v19 op_sel:[0,0,1]
	v_cvt_pk_fp8_f32 v10, v3, v16 op_sel:[0,0,1]
	v_mov_b32_e32 v3, v24
	v_mov_b32_e32 v12, v25
	v_cvt_pk_fp8_f32 v11, v3, v12 op_sel:[0,0,1]
	global_store_dwordx2 v[6:7], v[8:9], off
	global_store_dwordx2 v[6:7], v[10:11], off offset:2048
	v_add_u32_e32 v9, 0x80, v2
	v_ashrrev_i32_e32 v10, 4, v9
	v_ashrrev_i32_e32 v11, 31, v10
	v_lshlrev_b64 v[10:11], 18, v[10:11]
	v_lshl_add_u64 v[10:11], s[24:25], 0, v[10:11]
	v_lshl_add_u64 v[10:11], v[10:11], 0, s[20:21]
	v_lshl_add_u64 v[10:11], v[10:11], 0, v[172:173]
	v_lshl_add_u64 v[10:11], v[10:11], 0, v[170:171]
	v_fmamk_f32 v3, v238, 0x39800000, v194
	v_mul_f32_e32 v9, 0x4b800000, v3
	v_cmp_gt_f32_e32 vcc, s43, v3
	s_nop 1
	v_cndmask_b32_e32 v3, v3, v9, vcc
	v_rsq_f32_e32 v3, v3
	s_nop 0
	v_mul_f32_e32 v9, 0x45800000, v3
	v_cndmask_b32_e32 v3, v3, v9, vcc
	v_mul_f32_e32 v12, 0x3d000000, v3
	v_pk_mul_f32 v[16:17], v[94:95], v[12:13] op_sel_hi:[1,0]
	v_pk_mul_f32 v[20:21], v[90:91], v[12:13] op_sel_hi:[1,0]
; __device__ __forceinline__ unsigned pk4_fp8(float a, float b, float c, float d) {
;     a = fminf(fmaxf(a, -448.f), 448.f); b = fminf(fmaxf(b, -448.f), 448.f); c = fminf(fmaxf(c, -448.f), 448.f); d = fminf(fmaxf(d, -448.f), 448.f);
;     int w = 0; w = __builtin_amdgcn_cvt_pk_fp8_f32(a, b, w, false); w = __builtin_amdgcn_cvt_pk_fp8_f32(c, d, w, true); return (unsigned)w;
;     __device__ __forceinline__ void operator()(const f32x4 (&acc)[2][2][4][2], const Unit& u, int wr, int wc, int fr, int fq) const {
;         const int row0 = u.pm * BM + wr * 64 + fr, col0 = u.pn * BM + wc * 32 + 8 * fq;
; #pragma unroll
;         for (int ai = 0; ai < 2; ++ai)
; #pragma unroll
;             for (int m = 0; m < 4; ++m) {
;                 const int row = row0 + ai * HALF + m * 16;
;                 const float rs = rsqrtf(ss[row] * (1.0f / 4096.0f) + RMS_EPS) * (1.0f / 64.0f);
;                 unsigned char* rowp = U + ((size_t)(row >> 4) * 512 + (col0 >> 5)) * 512 + (row & 15) * 32 + (col0 & 31);
; #pragma unroll
;                 for (int bj = 0; bj < 2; ++bj) {
;                     f32x4 v0 = acc[ai][bj][m][0] * rs, v1 = acc[ai][bj][m][1] * rs;
; #pragma unroll
;                     for (int j = 0; j < 4; ++j) { const float a = fmaxf(v0[j], 0.f), b = fmaxf(v1[j], 0.f); v0[j] = a * a * 4.f; v1[j] = b * b * 4.f; }
;                     u32x2 w; w.x = pk4_fp8(v0[0], v0[1], v0[2], v0[3]); w.y = pk4_fp8(v1[0], v1[1], v1[2], v1[3]);
;                     *(u32x2*)(rowp + bj * (HALF / 32) * 512) = w;
;                 }
	v_pk_mul_f32 v[24:25], v[86:87], v[12:13] op_sel_hi:[1,0]
	v_pk_mul_f32 v[14:15], v[96:97], v[12:13] op_sel_hi:[1,0]
	v_pk_mul_f32 v[18:19], v[92:93], v[12:13] op_sel_hi:[1,0]
	v_pk_mul_f32 v[22:23], v[88:89], v[12:13] op_sel_hi:[1,0]
	v_pk_mul_f32 v[26:27], v[84:85], v[12:13] op_sel_hi:[1,0]
	v_pk_mul_f32 v[12:13], v[82:83], v[12:13] op_sel_hi:[1,0]
	v_med3_f32 v3, v16, 0, s99
	v_med3_f32 v9, v20, 0, s99
	v_med3_f32 v16, v17, 0, s99
	v_med3_f32 v17, v21, 0, s99
	v_med3_f32 v20, v24, 0, s99
	v_med3_f32 v21, v25, 0, s99
	v_med3_f32 v12, v12, 0, s99
	v_med3_f32 v13, v13, 0, s99
	v_mul_f32_e32 v3, v3, v3
	v_mul_f32_e32 v9, v9, v9
	v_mul_f32_e32 v16, v16, v16
	v_mul_f32_e32 v17, v17, v17
	v_mul_f32_e32 v20, v20, v20
	v_mul_f32_e32 v21, v21, v21
	v_mul_f32_e32 v12, v12, v12
	v_mul_f32_e32 v13, v13, v13
	v_med3_f32 v14, v14, 0, s99
	v_med3_f32 v18, v18, 0, s99
	v_med3_f32 v15, v15, 0, s99
	v_med3_f32 v19, v19, 0, s99
	v_med3_f32 v22, v22, 0, s99
	v_med3_f32 v23, v23, 0, s99
	v_cvt_pk_fp8_f32 v6, v3, v16
	v_cvt_pk_fp8_f32 v7, v9, v17
	v_cvt_pk_fp8_f32 v8, v20, v21
	v_med3_f32 v24, v26, 0, s99
	v_med3_f32 v25, v27, 0, s99
	v_mul_f32_e32 v14, v14, v14
	v_mul_f32_e32 v18, v18, v18
	v_mul_f32_e32 v15, v15, v15
	v_mul_f32_e32 v19, v19, v19
	v_mul_f32_e32 v22, v22, v22
	v_mul_f32_e32 v23, v23, v23
	v_cvt_pk_fp8_f32 v9, v12, v13
	v_mul_f32_e32 v24, v24, v24
	v_mul_f32_e32 v25, v25, v25
	v_mov_b32_e32 v3, v23
	v_cvt_pk_fp8_f32 v6, v14, v15 op_sel:[0,0,1]
	v_cvt_pk_fp8_f32 v7, v18, v19 op_sel:[0,0,1]
	v_cvt_pk_fp8_f32 v8, v22, v3 op_sel:[0,0,1]
	v_mov_b32_e32 v3, v24
	v_mov_b32_e32 v12, v25
	v_cvt_pk_fp8_f32 v9, v3, v12 op_sel:[0,0,1]
	global_store_dwordx2 v[10:11], v[6:7], off
	global_store_dwordx2 v[10:11], v[8:9], off offset:2048
	v_add_u32_e32 v9, 0x90, v2
	v_ashrrev_i32_e32 v10, 4, v9
	v_ashrrev_i32_e32 v11, 31, v10
	v_lshlrev_b64 v[10:11], 18, v[10:11]
	v_lshl_add_u64 v[10:11], s[24:25], 0, v[10:11]
	v_lshl_add_u64 v[10:11], v[10:11], 0, s[20:21]
	v_lshl_add_u64 v[10:11], v[10:11], 0, v[172:173]
	v_lshl_add_u64 v[10:11], v[10:11], 0, v[170:171]
	v_fmamk_f32 v3, v239, 0x39800000, v194
	v_mul_f32_e32 v9, 0x4b800000, v3
	v_cmp_gt_f32_e32 vcc, s43, v3
	s_nop 1
	v_cndmask_b32_e32 v3, v3, v9, vcc
	v_rsq_f32_e32 v3, v3
	s_nop 0
	v_mul_f32_e32 v9, 0x45800000, v3
	v_cndmask_b32_e32 v3, v3, v9, vcc
	v_mul_f32_e32 v12, 0x3d000000, v3
	v_pk_mul_f32 v[16:17], v[78:79], v[12:13] op_sel_hi:[1,0]
	v_pk_mul_f32 v[20:21], v[74:75], v[12:13] op_sel_hi:[1,0]
	v_pk_mul_f32 v[14:15], v[80:81], v[12:13] op_sel_hi:[1,0]
	v_pk_mul_f32 v[18:19], v[76:77], v[12:13] op_sel_hi:[1,0]
	v_pk_mul_f32 v[22:23], v[72:73], v[12:13] op_sel_hi:[1,0]
	v_pk_mul_f32 v[24:25], v[70:71], v[12:13] op_sel_hi:[1,0]
	v_pk_mul_f32 v[26:27], v[68:69], v[12:13] op_sel_hi:[1,0]
	v_pk_mul_f32 v[12:13], v[66:67], v[12:13] op_sel_hi:[1,0]
	v_med3_f32 v3, v16, 0, s99
	v_med3_f32 v9, v20, 0, s99
	v_med3_f32 v16, v17, 0, s99
	v_med3_f32 v17, v21, 0, s99
	v_med3_f32 v20, v24, 0, s99
	v_med3_f32 v12, v12, 0, s99
	v_med3_f32 v21, v25, 0, s99
	v_med3_f32 v13, v13, 0, s99
	v_mul_f32_e32 v3, v3, v3
	v_mul_f32_e32 v9, v9, v9
	v_mul_f32_e32 v16, v16, v16
	v_mul_f32_e32 v17, v17, v17
	v_mul_f32_e32 v20, v20, v20
	v_mul_f32_e32 v12, v12, v12
	v_mul_f32_e32 v21, v21, v21
	v_mul_f32_e32 v13, v13, v13
	v_med3_f32 v14, v14, 0, s99
	v_med3_f32 v18, v18, 0, s99
	v_med3_f32 v15, v15, 0, s99
	v_med3_f32 v19, v19, 0, s99
	v_cvt_pk_fp8_f32 v6, v3, v16
	v_cvt_pk_fp8_f32 v7, v9, v17
	v_mov_b32_e32 v3, v12
	v_mov_b32_e32 v12, v13
	v_med3_f32 v22, v22, 0, s99
	v_med3_f32 v24, v26, 0, s99
	v_med3_f32 v23, v23, 0, s99
	v_med3_f32 v25, v27, 0, s99
	v_mul_f32_e32 v14, v14, v14
	v_mul_f32_e32 v18, v18, v18
	v_mul_f32_e32 v15, v15, v15
	v_mul_f32_e32 v19, v19, v19
	v_cvt_pk_fp8_f32 v8, v20, v21
	v_cvt_pk_fp8_f32 v9, v3, v12
	v_mul_f32_e32 v22, v22, v22
	v_mul_f32_e32 v24, v24, v24
	v_mul_f32_e32 v23, v23, v23
	v_mul_f32_e32 v25, v25, v25
	v_cvt_pk_fp8_f32 v6, v14, v15 op_sel:[0,0,1]
	v_cvt_pk_fp8_f32 v7, v18, v19 op_sel:[0,0,1]
	v_mov_b32_e32 v3, v24
	v_mov_b32_e32 v12, v25
	v_cvt_pk_fp8_f32 v8, v22, v23 op_sel:[0,0,1]
	v_cvt_pk_fp8_f32 v9, v3, v12 op_sel:[0,0,1]
	global_store_dwordx2 v[10:11], v[6:7], off
	global_store_dwordx2 v[10:11], v[8:9], off offset:2048
	v_add_u32_e32 v9, 0xa0, v2
	v_ashrrev_i32_e32 v10, 4, v9
	v_ashrrev_i32_e32 v11, 31, v10
	v_lshlrev_b64 v[10:11], 18, v[10:11]
	v_lshl_add_u64 v[10:11], s[24:25], 0, v[10:11]
	v_lshl_add_u64 v[10:11], v[10:11], 0, s[20:21]
	v_lshl_add_u64 v[10:11], v[10:11], 0, v[172:173]
	v_lshl_add_u64 v[10:11], v[10:11], 0, v[170:171]
	v_add_u32_e32 v2, 0xb0, v2
	v_ashrrev_i32_e32 v2, 4, v2
; __device__ __forceinline__ unsigned pk4_fp8(float a, float b, float c, float d) {
;     a = fminf(fmaxf(a, -448.f), 448.f); b = fminf(fmaxf(b, -448.f), 448.f); c = fminf(fmaxf(c, -448.f), 448.f); d = fminf(fmaxf(d, -448.f), 448.f);
;     int w = 0; w = __builtin_amdgcn_cvt_pk_fp8_f32(a, b, w, false); w = __builtin_amdgcn_cvt_pk_fp8_f32(c, d, w, true); return (unsigned)w;
;     __device__ __forceinline__ void operator()(const f32x4 (&acc)[2][2][4][2], const Unit& u, int wr, int wc, int fr, int fq) const {
;         const int row0 = u.pm * BM + wr * 64 + fr, col0 = u.pn * BM + wc * 32 + 8 * fq;
; #pragma unroll
;         for (int ai = 0; ai < 2; ++ai)
; #pragma unroll
;             for (int m = 0; m < 4; ++m) {
;                 const int row = row0 + ai * HALF + m * 16;
;                 const float rs = rsqrtf(ss[row] * (1.0f / 4096.0f) + RMS_EPS) * (1.0f / 64.0f);
;                 unsigned char* rowp = U + ((size_t)(row >> 4) * 512 + (col0 >> 5)) * 512 + (row & 15) * 32 + (col0 & 31);
; #pragma unroll
;                 for (int bj = 0; bj < 2; ++bj) {
;                     f32x4 v0 = acc[ai][bj][m][0] * rs, v1 = acc[ai][bj][m][1] * rs;
; #pragma unroll
;                     for (int j = 0; j < 4; ++j) { const float a = fmaxf(v0[j], 0.f), b = fmaxf(v1[j], 0.f); v0[j] = a * a * 4.f; v1[j] = b * b * 4.f; }
;                     u32x2 w; w.x = pk4_fp8(v0[0], v0[1], v0[2], v0[3]); w.y = pk4_fp8(v1[0], v1[1], v1[2], v1[3]);
;                     *(u32x2*)(rowp + bj * (HALF / 32) * 512) = w;
;                 }
	v_fmamk_f32 v3, v240, 0x39800000, v194
	v_mul_f32_e32 v9, 0x4b800000, v3
	v_cmp_gt_f32_e32 vcc, s43, v3
	s_nop 1
	v_cndmask_b32_e32 v3, v3, v9, vcc
	v_rsq_f32_e32 v3, v3
	s_nop 0
	v_mul_f32_e32 v9, 0x45800000, v3
	v_cndmask_b32_e32 v3, v3, v9, vcc
	v_mul_f32_e32 v12, 0x3d000000, v3
	v_pk_mul_f32 v[16:17], v[62:63], v[12:13] op_sel_hi:[1,0]
	v_pk_mul_f32 v[20:21], v[58:59], v[12:13] op_sel_hi:[1,0]
	v_pk_mul_f32 v[14:15], v[64:65], v[12:13] op_sel_hi:[1,0]
	v_pk_mul_f32 v[18:19], v[60:61], v[12:13] op_sel_hi:[1,0]
	v_pk_mul_f32 v[22:23], v[56:57], v[12:13] op_sel_hi:[1,0]
	v_pk_mul_f32 v[24:25], v[54:55], v[12:13] op_sel_hi:[1,0]
	v_pk_mul_f32 v[26:27], v[52:53], v[12:13] op_sel_hi:[1,0]
	v_pk_mul_f32 v[12:13], v[50:51], v[12:13] op_sel_hi:[1,0]
	v_med3_f32 v3, v16, 0, s99
	v_med3_f32 v9, v20, 0, s99
	v_med3_f32 v16, v17, 0, s99
	v_med3_f32 v17, v21, 0, s99
	v_med3_f32 v20, v24, 0, s99
	v_med3_f32 v12, v12, 0, s99
	v_med3_f32 v21, v25, 0, s99
	v_med3_f32 v13, v13, 0, s99
	v_mul_f32_e32 v3, v3, v3
	v_mul_f32_e32 v9, v9, v9
	v_mul_f32_e32 v16, v16, v16
	v_mul_f32_e32 v17, v17, v17
	v_mul_f32_e32 v20, v20, v20
	v_mul_f32_e32 v12, v12, v12
	v_mul_f32_e32 v21, v21, v21
	v_mul_f32_e32 v13, v13, v13
	v_med3_f32 v14, v14, 0, s99
	v_med3_f32 v18, v18, 0, s99
	v_med3_f32 v15, v15, 0, s99
	v_med3_f32 v19, v19, 0, s99
	v_cvt_pk_fp8_f32 v6, v3, v16
	v_cvt_pk_fp8_f32 v7, v9, v17
	v_mov_b32_e32 v3, v13
	v_med3_f32 v22, v22, 0, s99
	v_med3_f32 v24, v26, 0, s99
	v_med3_f32 v23, v23, 0, s99
	v_med3_f32 v25, v27, 0, s99
	v_mul_f32_e32 v14, v14, v14
	v_mul_f32_e32 v18, v18, v18
	v_mul_f32_e32 v15, v15, v15
	v_mul_f32_e32 v19, v19, v19
	v_cvt_pk_fp8_f32 v8, v20, v21
	v_cvt_pk_fp8_f32 v9, v12, v3
	v_mul_f32_e32 v22, v22, v22
	v_mul_f32_e32 v24, v24, v24
	v_mul_f32_e32 v23, v23, v23
	v_mul_f32_e32 v25, v25, v25
	v_cvt_pk_fp8_f32 v6, v14, v15 op_sel:[0,0,1]
	v_cvt_pk_fp8_f32 v7, v18, v19 op_sel:[0,0,1]
	v_mov_b32_e32 v3, v24
	v_mov_b32_e32 v12, v25
	v_cvt_pk_fp8_f32 v8, v22, v23 op_sel:[0,0,1]
	v_cvt_pk_fp8_f32 v9, v3, v12 op_sel:[0,0,1]
	global_store_dwordx2 v[10:11], v[6:7], off
	global_store_dwordx2 v[10:11], v[8:9], off offset:2048
	v_ashrrev_i32_e32 v3, 31, v2
	v_lshlrev_b64 v[2:3], 18, v[2:3]
	v_lshl_add_u64 v[2:3], s[24:25], 0, v[2:3]
	v_lshl_add_u64 v[2:3], v[2:3], 0, s[20:21]
	v_lshl_add_u64 v[2:3], v[2:3], 0, v[172:173]
	v_lshl_add_u64 v[2:3], v[2:3], 0, v[170:171]
	v_fmamk_f32 v8, v241, 0x39800000, v194
	v_mul_f32_e32 v9, 0x4b800000, v8
	v_cmp_gt_f32_e32 vcc, s43, v8
	s_nop 1
	v_cndmask_b32_e32 v8, v8, v9, vcc
	v_rsq_f32_e32 v8, v8
	s_nop 0
	v_mul_f32_e32 v9, 0x45800000, v8
	v_cndmask_b32_e32 v8, v8, v9, vcc
	v_mul_f32_e32 v8, 0x3d000000, v8
	v_pk_mul_f32 v[12:13], v[46:47], v[8:9] op_sel_hi:[1,0]
	v_pk_mul_f32 v[16:17], v[42:43], v[8:9] op_sel_hi:[1,0]
	v_pk_mul_f32 v[10:11], v[48:49], v[8:9] op_sel_hi:[1,0]
	v_pk_mul_f32 v[14:15], v[44:45], v[8:9] op_sel_hi:[1,0]
	v_pk_mul_f32 v[18:19], v[40:41], v[8:9] op_sel_hi:[1,0]
	v_pk_mul_f32 v[20:21], v[38:39], v[8:9] op_sel_hi:[1,0]
	v_pk_mul_f32 v[22:23], v[36:37], v[8:9] op_sel_hi:[1,0]
	v_pk_mul_f32 v[8:9], v[34:35], v[8:9] op_sel_hi:[1,0]
	v_med3_f32 v12, v12, 0, s99
	v_med3_f32 v16, v16, 0, s99
	v_med3_f32 v13, v13, 0, s99
	v_med3_f32 v17, v17, 0, s99
	v_med3_f32 v20, v20, 0, s99
	v_med3_f32 v8, v8, 0, s99
	v_med3_f32 v21, v21, 0, s99
	v_med3_f32 v9, v9, 0, s99
	v_mul_f32_e32 v12, v12, v12
	v_mul_f32_e32 v16, v16, v16
	v_mul_f32_e32 v13, v13, v13
	v_mul_f32_e32 v17, v17, v17
	v_mul_f32_e32 v20, v20, v20
	v_mul_f32_e32 v8, v8, v8
	v_mul_f32_e32 v21, v21, v21
	v_mul_f32_e32 v9, v9, v9
	v_med3_f32 v10, v10, 0, s99
	v_med3_f32 v14, v14, 0, s99
	v_med3_f32 v11, v11, 0, s99
	v_med3_f32 v15, v15, 0, s99
	v_cvt_pk_fp8_f32 v4, v12, v13
	v_cvt_pk_fp8_f32 v5, v16, v17
	v_med3_f32 v18, v18, 0, s99
	v_med3_f32 v22, v22, 0, s99
	v_med3_f32 v19, v19, 0, s99
	v_med3_f32 v23, v23, 0, s99
	v_mul_f32_e32 v10, v10, v10
	v_mul_f32_e32 v14, v14, v14
	v_mul_f32_e32 v11, v11, v11
	v_mul_f32_e32 v15, v15, v15
	v_cvt_pk_fp8_f32 v6, v20, v21
	v_cvt_pk_fp8_f32 v7, v8, v9
	v_mul_f32_e32 v18, v18, v18
	v_mul_f32_e32 v22, v22, v22
	v_mul_f32_e32 v19, v19, v19
	v_mul_f32_e32 v23, v23, v23
	v_cvt_pk_fp8_f32 v4, v10, v11 op_sel:[0,0,1]
	v_cvt_pk_fp8_f32 v5, v14, v15 op_sel:[0,0,1]
	v_mov_b32_e32 v8, v22
	v_mov_b32_e32 v9, v23
	v_cvt_pk_fp8_f32 v6, v18, v19 op_sel:[0,0,1]
	v_cvt_pk_fp8_f32 v7, v8, v9 op_sel:[0,0,1]
	s_andn2_b64 vcc, exec, s[0:1]
	s_mov_b64 s[0:1], -1
	global_store_dwordx2 v[2:3], v[4:5], off
	global_store_dwordx2 v[2:3], v[6:7], off offset:2048
	s_cbranch_vccnz .LBB0_2273
	s_andn2_b64 vcc, exec, s[4:5]
	s_cbranch_vccnz .LBB0_2272
	s_barrier
	s_branch .LBB0_2272
